# E1 epilogue: rows (m, m+1) paired by v_permlane16_swap so the write-through activation stores are 4 x dwordx4 instead of 8 x dwordx2 per wave
# speedup vs baseline: 1.0157x; 1.0034x over previous
.LBB0_1064:
	v_mbcnt_lo_u32_b32 v226, -1, 0
	v_mbcnt_hi_u32_b32 v226, -1, v226
	v_and_b32_e32 v226, 16, v226
	v_mul_f32_e32 v4, 0xbd38aa3b, v158
	v_exp_f32_e32 v7, v4
	v_mul_f32_e32 v4, 0xbd38aa3b, v150
	v_exp_f32_e32 v11, v4
	v_mul_f32_e32 v4, 0xbd38aa3b, v159
	v_exp_f32_e32 v13, v4
	v_mul_f32_e32 v4, 0xbd38aa3b, v151
	v_exp_f32_e32 v14, v4
	v_mul_f32_e32 v4, 0xbd38aa3b, v160
	v_exp_f32_e32 v15, v4
	v_mul_f32_e32 v4, 0xbd38aa3b, v152
	v_fmamk_f32 v7, v7, 0x44800000, v213
	v_exp_f32_e32 v16, v4
	v_mul_f32_e32 v4, 0xbd38aa3b, v161
	v_rcp_f32_e32 v10, v7
	v_fmamk_f32 v7, v11, 0x44800000, v213
	v_exp_f32_e32 v17, v4
	v_mul_f32_e32 v4, 0xbd38aa3b, v153
	v_rcp_f32_e32 v12, v7
	v_fmamk_f32 v7, v13, 0x44800000, v213
	v_exp_f32_e32 v18, v4
	v_rcp_f32_e32 v11, v7
	v_fmamk_f32 v7, v14, 0x44800000, v213
	v_rcp_f32_e32 v13, v7
	v_fmamk_f32 v7, v15, 0x44800000, v213
	v_rcp_f32_e32 v14, v7
	v_fmamk_f32 v7, v16, 0x44800000, v213
	v_rcp_f32_e32 v16, v7
	v_fmamk_f32 v7, v17, 0x44800000, v213
	v_pk_mul_f32 v[8:9], v[158:159], v[154:155]
	v_rcp_f32_e32 v15, v7
	v_fmamk_f32 v7, v18, 0x44800000, v213
	v_pk_mul_f32 v[20:21], v[150:151], v[146:147]
	v_rcp_f32_e32 v17, v7
	v_pk_mul_f32 v[8:9], v[8:9], v[10:11]
	v_pk_mul_f32 v[10:11], v[20:21], v[12:13]
	v_mov_b32_e32 v12, v0
	v_mov_b32_e32 v13, v0
	v_cvt_pk_fp8_f32 v12, v8, v9
	v_cvt_pk_fp8_f32 v13, v10, v11
	v_pk_mul_f32 v[4:5], v[160:161], v[156:157]
	v_pk_mul_f32 v[18:19], v[152:153], v[148:149]
	v_pk_mul_f32 v[4:5], v[4:5], v[14:15]
	v_pk_mul_f32 v[8:9], v[18:19], v[16:17]
	v_cvt_pk_fp8_f32 v12, v4, v5 op_sel:[0,0,1]
	v_cvt_pk_fp8_f32 v13, v8, v9 op_sel:[0,0,1]
	v_lshl_or_b32 v2, s86, 7, v173
	v_lshl_add_u32 v6, s87, 8, v196
	v_mov_b64_e32 v[4:5], s[84:85]
	v_ashrrev_i32_e32 v3, 31, v2
	v_mad_i64_i32 v[8:9], s[18:19], v6, s57, v[4:5]
	v_lshl_add_u64 v[8:9], v[8:9], 0, v[2:3]
	v_mul_f32_e32 v7, 0xbd38aa3b, v142
	s_nop 15
	s_nop 15
	v_mov_b32_e32 v220, v12
	v_mov_b32_e32 v221, v13
	v_mov_b32_e32 v218, v8
	v_mov_b32_e32 v219, v9
	v_exp_f32_e32 v7, v7
	v_mul_f32_e32 v8, 0xbd38aa3b, v134
	v_exp_f32_e32 v13, v8
	v_mul_f32_e32 v8, 0xbd38aa3b, v143
	v_exp_f32_e32 v15, v8
	v_mul_f32_e32 v8, 0xbd38aa3b, v135
	v_exp_f32_e32 v16, v8
	v_mul_f32_e32 v8, 0xbd38aa3b, v144
	v_exp_f32_e32 v17, v8
	v_mul_f32_e32 v8, 0xbd38aa3b, v136
	v_fmamk_f32 v7, v7, 0x44800000, v213
	v_exp_f32_e32 v18, v8
	v_mul_f32_e32 v8, 0xbd38aa3b, v145
	v_rcp_f32_e32 v12, v7
	v_fmamk_f32 v7, v13, 0x44800000, v213
	v_exp_f32_e32 v19, v8
	v_mul_f32_e32 v8, 0xbd38aa3b, v137
	v_rcp_f32_e32 v14, v7
	v_fmamk_f32 v7, v15, 0x44800000, v213
	v_exp_f32_e32 v20, v8
	v_rcp_f32_e32 v13, v7
	v_fmamk_f32 v7, v16, 0x44800000, v213
	v_rcp_f32_e32 v15, v7
	v_fmamk_f32 v7, v17, 0x44800000, v213
	v_rcp_f32_e32 v16, v7
	v_fmamk_f32 v7, v18, 0x44800000, v213
	v_rcp_f32_e32 v18, v7
	v_fmamk_f32 v7, v19, 0x44800000, v213
	v_pk_mul_f32 v[10:11], v[142:143], v[138:139]
	v_rcp_f32_e32 v17, v7
	v_fmamk_f32 v7, v20, 0x44800000, v213
	v_pk_mul_f32 v[22:23], v[134:135], v[130:131]
	v_rcp_f32_e32 v19, v7
	v_pk_mul_f32 v[10:11], v[10:11], v[12:13]
	v_pk_mul_f32 v[12:13], v[22:23], v[14:15]
	v_mov_b32_e32 v14, v0
	v_mov_b32_e32 v15, v0
	v_cvt_pk_fp8_f32 v14, v10, v11
	v_cvt_pk_fp8_f32 v15, v12, v13
	v_pk_mul_f32 v[8:9], v[144:145], v[140:141]
	v_pk_mul_f32 v[20:21], v[136:137], v[132:133]
	v_pk_mul_f32 v[8:9], v[8:9], v[16:17]
	v_pk_mul_f32 v[10:11], v[20:21], v[18:19]
	v_cvt_pk_fp8_f32 v14, v8, v9 op_sel:[0,0,1]
	v_cvt_pk_fp8_f32 v15, v10, v11 op_sel:[0,0,1]
	v_or_b32_e32 v7, 16, v6
	v_mad_i64_i32 v[8:9], s[18:19], v7, s57, v[4:5]
	v_lshl_add_u64 v[8:9], v[8:9], 0, v[2:3]
	v_mul_f32_e32 v7, 0xbd38aa3b, v126
	v_mov_b32_e32 v222, v14
	v_mov_b32_e32 v223, v15
	v_lshl_add_u64 v[224:225], v[8:9], 0, -8
	v_cmp_ne_u32_e64 s[18:19], 0, v226
	s_nop 1
	v_permlane16_swap_b32_e32 v220, v222
	v_permlane16_swap_b32_e32 v221, v223
	v_cndmask_b32_e64 v224, v218, v224, s[18:19]
	v_cndmask_b32_e64 v225, v219, v225, s[18:19]
	global_store_dwordx4 v[224:225], v[220:223], off sc1
	v_exp_f32_e32 v7, v7
	v_mul_f32_e32 v8, 0xbd38aa3b, v118
	v_exp_f32_e32 v13, v8
	v_mul_f32_e32 v8, 0xbd38aa3b, v127
	v_exp_f32_e32 v15, v8
	v_mul_f32_e32 v8, 0xbd38aa3b, v119
	v_exp_f32_e32 v16, v8
	v_mul_f32_e32 v8, 0xbd38aa3b, v128
	v_exp_f32_e32 v17, v8
	v_mul_f32_e32 v8, 0xbd38aa3b, v120
	v_fmamk_f32 v7, v7, 0x44800000, v213
	v_exp_f32_e32 v18, v8
	v_mul_f32_e32 v8, 0xbd38aa3b, v129
	v_rcp_f32_e32 v12, v7
	v_fmamk_f32 v7, v13, 0x44800000, v213
	v_exp_f32_e32 v19, v8
	v_mul_f32_e32 v8, 0xbd38aa3b, v121
	v_rcp_f32_e32 v14, v7
	v_fmamk_f32 v7, v15, 0x44800000, v213
	v_exp_f32_e32 v20, v8
	v_rcp_f32_e32 v13, v7
	v_fmamk_f32 v7, v16, 0x44800000, v213
	v_rcp_f32_e32 v15, v7
	v_fmamk_f32 v7, v17, 0x44800000, v213
	v_rcp_f32_e32 v16, v7
	v_fmamk_f32 v7, v18, 0x44800000, v213
	v_rcp_f32_e32 v18, v7
	v_fmamk_f32 v7, v19, 0x44800000, v213
	v_pk_mul_f32 v[10:11], v[126:127], v[122:123]
	v_rcp_f32_e32 v17, v7
	v_fmamk_f32 v7, v20, 0x44800000, v213
	v_pk_mul_f32 v[22:23], v[118:119], v[114:115]
	v_rcp_f32_e32 v19, v7
	v_pk_mul_f32 v[10:11], v[10:11], v[12:13]
	v_pk_mul_f32 v[12:13], v[22:23], v[14:15]
	v_mov_b32_e32 v14, v0
	v_mov_b32_e32 v15, v0
	v_cvt_pk_fp8_f32 v14, v10, v11
	v_cvt_pk_fp8_f32 v15, v12, v13
	v_pk_mul_f32 v[8:9], v[128:129], v[124:125]
	v_pk_mul_f32 v[20:21], v[120:121], v[116:117]
	v_pk_mul_f32 v[8:9], v[8:9], v[16:17]
	v_pk_mul_f32 v[10:11], v[20:21], v[18:19]
	v_cvt_pk_fp8_f32 v14, v8, v9 op_sel:[0,0,1]
	v_cvt_pk_fp8_f32 v15, v10, v11 op_sel:[0,0,1]
	v_or_b32_e32 v7, 32, v6
	v_mad_i64_i32 v[8:9], s[18:19], v7, s57, v[4:5]
	v_lshl_add_u64 v[8:9], v[8:9], 0, v[2:3]
	v_mul_f32_e32 v7, 0xbd38aa3b, v110
	v_mov_b32_e32 v220, v14
	v_mov_b32_e32 v221, v15
	v_mov_b32_e32 v218, v8
	v_mov_b32_e32 v219, v9
	v_exp_f32_e32 v7, v7
	v_mul_f32_e32 v8, 0xbd38aa3b, v102
	v_exp_f32_e32 v13, v8
	v_mul_f32_e32 v8, 0xbd38aa3b, v111
	v_exp_f32_e32 v15, v8
	v_mul_f32_e32 v8, 0xbd38aa3b, v103
	v_exp_f32_e32 v16, v8
	v_mul_f32_e32 v8, 0xbd38aa3b, v112
	v_exp_f32_e32 v17, v8
	v_mul_f32_e32 v8, 0xbd38aa3b, v104
	v_fmamk_f32 v7, v7, 0x44800000, v213
	v_exp_f32_e32 v18, v8
	v_mul_f32_e32 v8, 0xbd38aa3b, v113
	v_rcp_f32_e32 v12, v7
	v_fmamk_f32 v7, v13, 0x44800000, v213
	v_exp_f32_e32 v19, v8
	v_mul_f32_e32 v8, 0xbd38aa3b, v105
	v_rcp_f32_e32 v14, v7
	v_fmamk_f32 v7, v15, 0x44800000, v213
	v_exp_f32_e32 v20, v8
	v_rcp_f32_e32 v13, v7
	v_fmamk_f32 v7, v16, 0x44800000, v213
	v_rcp_f32_e32 v15, v7
	v_fmamk_f32 v7, v17, 0x44800000, v213
	v_rcp_f32_e32 v16, v7
	v_fmamk_f32 v7, v18, 0x44800000, v213
	v_rcp_f32_e32 v18, v7
	v_fmamk_f32 v7, v19, 0x44800000, v213
	v_pk_mul_f32 v[10:11], v[110:111], v[106:107]
	v_rcp_f32_e32 v17, v7
	v_fmamk_f32 v7, v20, 0x44800000, v213
	v_pk_mul_f32 v[22:23], v[102:103], v[98:99]
	v_rcp_f32_e32 v19, v7
	v_pk_mul_f32 v[10:11], v[10:11], v[12:13]
	v_pk_mul_f32 v[12:13], v[22:23], v[14:15]
	v_mov_b32_e32 v14, v0
	v_mov_b32_e32 v15, v0
	v_cvt_pk_fp8_f32 v14, v10, v11
	v_cvt_pk_fp8_f32 v15, v12, v13
	v_pk_mul_f32 v[8:9], v[112:113], v[108:109]
	v_pk_mul_f32 v[20:21], v[104:105], v[100:101]
	v_pk_mul_f32 v[8:9], v[8:9], v[16:17]
	v_pk_mul_f32 v[10:11], v[20:21], v[18:19]
	v_cvt_pk_fp8_f32 v14, v8, v9 op_sel:[0,0,1]
	v_cvt_pk_fp8_f32 v15, v10, v11 op_sel:[0,0,1]
	v_or_b32_e32 v7, 48, v6
	v_mad_i64_i32 v[8:9], s[18:19], v7, s57, v[4:5]
	v_lshl_add_u64 v[8:9], v[8:9], 0, v[2:3]
	v_mov_b32_e32 v222, v14
	v_mov_b32_e32 v223, v15
	v_lshl_add_u64 v[224:225], v[8:9], 0, -8
	v_cmp_ne_u32_e64 s[18:19], 0, v226
	s_nop 1
	v_permlane16_swap_b32_e32 v220, v222
	v_permlane16_swap_b32_e32 v221, v223
	v_cndmask_b32_e64 v224, v218, v224, s[18:19]
	v_cndmask_b32_e64 v225, v219, v225, s[18:19]
	global_store_dwordx4 v[224:225], v[220:223], off sc1
	v_mul_f32_e32 v8, 0xbd38aa3b, v94
	v_exp_f32_e32 v12, v8
	v_mul_f32_e32 v8, 0xbd38aa3b, v86
	v_exp_f32_e32 v13, v8
	v_mul_f32_e32 v8, 0xbd38aa3b, v95
	v_exp_f32_e32 v15, v8
	v_mul_f32_e32 v8, 0xbd38aa3b, v87
	v_exp_f32_e32 v16, v8
	v_mul_f32_e32 v8, 0xbd38aa3b, v96
	v_exp_f32_e32 v17, v8
	v_mul_f32_e32 v8, 0xbd38aa3b, v88
	v_exp_f32_e32 v18, v8
	v_mul_f32_e32 v8, 0xbd38aa3b, v97
	v_exp_f32_e32 v19, v8
	v_mul_f32_e32 v8, 0xbd38aa3b, v89
	v_fmamk_f32 v13, v13, 0x44800000, v213
	v_exp_f32_e32 v20, v8
	v_fmamk_f32 v12, v12, 0x44800000, v213
	v_rcp_f32_e32 v14, v13
	v_fmamk_f32 v13, v15, 0x44800000, v213
	v_fmamk_f32 v15, v16, 0x44800000, v213
	v_rcp_f32_e32 v12, v12
	v_rcp_f32_e32 v13, v13
	v_rcp_f32_e32 v15, v15
	v_fmamk_f32 v16, v17, 0x44800000, v213
	v_fmamk_f32 v17, v18, 0x44800000, v213
	v_pk_mul_f32 v[10:11], v[94:95], v[90:91]
	v_rcp_f32_e32 v18, v17
	v_fmamk_f32 v17, v19, 0x44800000, v213
	v_fmamk_f32 v19, v20, 0x44800000, v213
	v_pk_mul_f32 v[22:23], v[86:87], v[82:83]
	v_rcp_f32_e32 v16, v16
	v_rcp_f32_e32 v17, v17
	v_rcp_f32_e32 v19, v19
	v_pk_mul_f32 v[10:11], v[10:11], v[12:13]
	v_pk_mul_f32 v[12:13], v[22:23], v[14:15]
	v_mov_b32_e32 v14, v0
	v_mov_b32_e32 v15, v0
	v_cvt_pk_fp8_f32 v14, v10, v11
	v_cvt_pk_fp8_f32 v15, v12, v13
	v_pk_mul_f32 v[8:9], v[96:97], v[92:93]
	v_pk_mul_f32 v[20:21], v[88:89], v[84:85]
	v_pk_mul_f32 v[8:9], v[8:9], v[16:17]
	v_pk_mul_f32 v[10:11], v[20:21], v[18:19]
	v_cvt_pk_fp8_f32 v14, v8, v9 op_sel:[0,0,1]
	v_cvt_pk_fp8_f32 v15, v10, v11 op_sel:[0,0,1]
	v_add_u32_e32 v7, 0x80, v6
	v_mad_i64_i32 v[8:9], s[18:19], v7, s57, v[4:5]
	v_lshl_add_u64 v[8:9], v[8:9], 0, v[2:3]
	v_mul_f32_e32 v7, 0xbd38aa3b, v78
	v_mov_b32_e32 v220, v14
	v_mov_b32_e32 v221, v15
	v_mov_b32_e32 v218, v8
	v_mov_b32_e32 v219, v9
	v_exp_f32_e32 v7, v7
	v_mul_f32_e32 v8, 0xbd38aa3b, v62
	v_exp_f32_e32 v13, v8
	v_mul_f32_e32 v8, 0xbd38aa3b, v79
	v_exp_f32_e32 v15, v8
	v_mul_f32_e32 v8, 0xbd38aa3b, v63
	v_exp_f32_e32 v16, v8
	v_mul_f32_e32 v8, 0xbd38aa3b, v80
	v_exp_f32_e32 v17, v8
	v_mul_f32_e32 v8, 0xbd38aa3b, v64
	v_fmamk_f32 v7, v7, 0x44800000, v213
	v_exp_f32_e32 v18, v8
	v_mul_f32_e32 v8, 0xbd38aa3b, v81
	v_rcp_f32_e32 v12, v7
	v_fmamk_f32 v7, v13, 0x44800000, v213
	v_exp_f32_e32 v19, v8
	v_mul_f32_e32 v8, 0xbd38aa3b, v65
	v_rcp_f32_e32 v14, v7
	v_fmamk_f32 v7, v15, 0x44800000, v213
	v_exp_f32_e32 v20, v8
	v_rcp_f32_e32 v13, v7
	v_fmamk_f32 v7, v16, 0x44800000, v213
	v_rcp_f32_e32 v15, v7
	v_fmamk_f32 v7, v17, 0x44800000, v213
	v_rcp_f32_e32 v16, v7
	v_fmamk_f32 v7, v18, 0x44800000, v213
	v_rcp_f32_e32 v18, v7
	v_fmamk_f32 v7, v19, 0x44800000, v213
	v_pk_mul_f32 v[10:11], v[78:79], v[74:75]
	v_rcp_f32_e32 v17, v7
	v_fmamk_f32 v7, v20, 0x44800000, v213
	v_pk_mul_f32 v[22:23], v[62:63], v[58:59]
	v_rcp_f32_e32 v19, v7
	v_pk_mul_f32 v[10:11], v[10:11], v[12:13]
	v_pk_mul_f32 v[12:13], v[22:23], v[14:15]
	v_mov_b32_e32 v14, v0
	v_mov_b32_e32 v15, v0
	v_cvt_pk_fp8_f32 v14, v10, v11
	v_cvt_pk_fp8_f32 v15, v12, v13
	v_pk_mul_f32 v[8:9], v[80:81], v[76:77]
	v_pk_mul_f32 v[20:21], v[64:65], v[60:61]
	v_pk_mul_f32 v[8:9], v[8:9], v[16:17]
	v_pk_mul_f32 v[10:11], v[20:21], v[18:19]
	v_cvt_pk_fp8_f32 v14, v8, v9 op_sel:[0,0,1]
	v_cvt_pk_fp8_f32 v15, v10, v11 op_sel:[0,0,1]
	v_add_u32_e32 v7, 0x90, v6
	v_mad_i64_i32 v[8:9], s[18:19], v7, s57, v[4:5]
	v_lshl_add_u64 v[8:9], v[8:9], 0, v[2:3]
	v_mul_f32_e32 v7, 0xbd38aa3b, v50
	v_mov_b32_e32 v222, v14
	v_mov_b32_e32 v223, v15
	v_lshl_add_u64 v[224:225], v[8:9], 0, -8
	v_cmp_ne_u32_e64 s[18:19], 0, v226
	s_nop 1
	v_permlane16_swap_b32_e32 v220, v222
	v_permlane16_swap_b32_e32 v221, v223
	v_cndmask_b32_e64 v224, v218, v224, s[18:19]
	v_cndmask_b32_e64 v225, v219, v225, s[18:19]
	global_store_dwordx4 v[224:225], v[220:223], off sc1
	v_exp_f32_e32 v7, v7
	v_mul_f32_e32 v8, 0xbd38aa3b, v66
	v_exp_f32_e32 v13, v8
	v_mul_f32_e32 v8, 0xbd38aa3b, v51
	v_exp_f32_e32 v15, v8
	v_mul_f32_e32 v8, 0xbd38aa3b, v67
	v_exp_f32_e32 v16, v8
	v_mul_f32_e32 v8, 0xbd38aa3b, v52
	v_exp_f32_e32 v17, v8
	v_mul_f32_e32 v8, 0xbd38aa3b, v68
	v_fmamk_f32 v7, v7, 0x44800000, v213
	v_exp_f32_e32 v18, v8
	v_mul_f32_e32 v8, 0xbd38aa3b, v53
	v_rcp_f32_e32 v12, v7
	v_fmamk_f32 v7, v13, 0x44800000, v213
	v_exp_f32_e32 v19, v8
	v_mul_f32_e32 v8, 0xbd38aa3b, v69
	v_rcp_f32_e32 v14, v7
	v_fmamk_f32 v7, v15, 0x44800000, v213
	v_exp_f32_e32 v20, v8
	v_rcp_f32_e32 v13, v7
	v_fmamk_f32 v7, v16, 0x44800000, v213
	v_rcp_f32_e32 v15, v7
	v_fmamk_f32 v7, v17, 0x44800000, v213
	v_rcp_f32_e32 v16, v7
	v_fmamk_f32 v7, v18, 0x44800000, v213
	v_rcp_f32_e32 v18, v7
	v_fmamk_f32 v7, v19, 0x44800000, v213
	v_pk_mul_f32 v[10:11], v[50:51], v[42:43]
	v_rcp_f32_e32 v17, v7
	v_fmamk_f32 v7, v20, 0x44800000, v213
	v_pk_mul_f32 v[22:23], v[66:67], v[70:71]
	v_rcp_f32_e32 v19, v7
	v_pk_mul_f32 v[10:11], v[10:11], v[12:13]
	v_pk_mul_f32 v[12:13], v[22:23], v[14:15]
	v_mov_b32_e32 v14, v0
	v_mov_b32_e32 v15, v0
	v_cvt_pk_fp8_f32 v14, v10, v11
	v_cvt_pk_fp8_f32 v15, v12, v13
	v_pk_mul_f32 v[8:9], v[52:53], v[44:45]
	v_pk_mul_f32 v[20:21], v[68:69], v[72:73]
	v_pk_mul_f32 v[8:9], v[8:9], v[16:17]
	v_pk_mul_f32 v[10:11], v[20:21], v[18:19]
	v_cvt_pk_fp8_f32 v14, v8, v9 op_sel:[0,0,1]
	v_cvt_pk_fp8_f32 v15, v10, v11 op_sel:[0,0,1]
	v_add_u32_e32 v7, 0xa0, v6
	v_mad_i64_i32 v[8:9], s[18:19], v7, s57, v[4:5]
	v_lshl_add_u64 v[8:9], v[8:9], 0, v[2:3]
	v_mul_f32_e32 v7, 0xbd38aa3b, v38
	v_mov_b32_e32 v220, v14
	v_mov_b32_e32 v221, v15
	v_mov_b32_e32 v218, v8
	v_mov_b32_e32 v219, v9
	v_exp_f32_e32 v7, v7
	v_mul_f32_e32 v8, 0xbd38aa3b, v46
	v_exp_f32_e32 v13, v8
	v_mul_f32_e32 v8, 0xbd38aa3b, v39
	v_exp_f32_e32 v15, v8
	v_mul_f32_e32 v8, 0xbd38aa3b, v47
	v_exp_f32_e32 v16, v8
	v_mul_f32_e32 v8, 0xbd38aa3b, v40
	v_exp_f32_e32 v17, v8
	v_mul_f32_e32 v8, 0xbd38aa3b, v48
	v_fmamk_f32 v7, v7, 0x44800000, v213
	v_exp_f32_e32 v18, v8
	v_mul_f32_e32 v8, 0xbd38aa3b, v41
	v_rcp_f32_e32 v12, v7
	v_fmamk_f32 v7, v13, 0x44800000, v213
	v_exp_f32_e32 v19, v8
	v_mul_f32_e32 v8, 0xbd38aa3b, v49
	v_rcp_f32_e32 v14, v7
	v_fmamk_f32 v7, v15, 0x44800000, v213
	v_exp_f32_e32 v20, v8
	v_rcp_f32_e32 v13, v7
	v_fmamk_f32 v7, v16, 0x44800000, v213
	v_rcp_f32_e32 v15, v7
	v_fmamk_f32 v7, v17, 0x44800000, v213
	v_rcp_f32_e32 v16, v7
	v_fmamk_f32 v7, v18, 0x44800000, v213
	v_rcp_f32_e32 v18, v7
	v_fmamk_f32 v7, v19, 0x44800000, v213
	v_pk_mul_f32 v[10:11], v[38:39], v[34:35]
	v_rcp_f32_e32 v17, v7
	v_fmamk_f32 v7, v20, 0x44800000, v213
	v_pk_mul_f32 v[22:23], v[46:47], v[54:55]
	v_rcp_f32_e32 v19, v7
	v_pk_mul_f32 v[10:11], v[10:11], v[12:13]
	v_pk_mul_f32 v[12:13], v[22:23], v[14:15]
	v_mov_b32_e32 v14, v0
	v_mov_b32_e32 v15, v0
	v_cvt_pk_fp8_f32 v14, v10, v11
	v_cvt_pk_fp8_f32 v15, v12, v13
	v_pk_mul_f32 v[8:9], v[40:41], v[36:37]
	v_pk_mul_f32 v[20:21], v[48:49], v[56:57]
	v_pk_mul_f32 v[8:9], v[8:9], v[16:17]
	v_pk_mul_f32 v[10:11], v[20:21], v[18:19]
	v_cvt_pk_fp8_f32 v14, v8, v9 op_sel:[0,0,1]
	v_cvt_pk_fp8_f32 v15, v10, v11 op_sel:[0,0,1]
	v_add_u32_e32 v6, 0xb0, v6
	v_mad_i64_i32 v[4:5], s[18:19], v6, s57, v[4:5]
	v_lshl_add_u64 v[2:3], v[4:5], 0, v[2:3]
	s_mov_b64 s[88:89], -1
	s_and_b64 vcc, exec, s[4:5]
	s_mov_b64 s[4:5], -1
	v_mov_b32_e32 v222, v14
	v_mov_b32_e32 v223, v15
	v_lshl_add_u64 v[224:225], v[2:3], 0, -8
	v_cmp_ne_u32_e64 s[18:19], 0, v226
	s_nop 1
	v_permlane16_swap_b32_e32 v220, v222
	v_permlane16_swap_b32_e32 v221, v223
	v_cndmask_b32_e64 v224, v218, v224, s[18:19]
	v_cndmask_b32_e64 v225, v219, v225, s[18:19]
	global_store_dwordx4 v[224:225], v[220:223], off sc1
	s_cbranch_vccnz .LBB0_1068
	s_andn2_b64 vcc, exec, s[14:15]
	s_cbranch_vccnz .LBB0_1067
	s_barrier
